# speedup vs baseline: 1.0527x; 1.0310x over previous
.LBB0_89:
	s_or_b64 exec, exec, s[8:9]
	v_mov_b32_e32 v3, 0
	v_lshlrev_b32_e32 v70, 4, v28
	s_and_saveexec_b64 s[60:61], vcc
	s_cbranch_execz .LBB0_118
	s_mov_b64 s[92:93], s[14:15]
	v_lshl_add_u64 v[22:23], s[12:13], 0, v[2:3]
	s_waitcnt vmcnt(0)
	v_cndmask_b32_e64 v55, -1, v4, s[0:1]
	s_movk_i32 s0, 0x880
	v_mov_b32_e32 v2, 0x1dd00
	v_mad_u32_u24 v4, v80, s0, v2
	v_lshlrev_b32_e32 v2, 1, v1
	v_mov_b32_e32 v27, v3
	v_mbcnt_hi_u32_b32 v2, -1, v29
	v_lshl_add_u64 v[72:73], v[22:23], 0, v[26:27]
	v_and_b32_e32 v23, 64, v2
	v_xor_b32_e32 v22, 16, v2
	v_add_u32_e32 v23, 64, v23
	v_cmp_lt_i32_e32 vcc, v22, v23
	v_lshlrev_b32_e32 v88, 2, v28
	v_and_b32_e32 v24, 7, v0
	v_cndmask_b32_e32 v22, v2, v22, vcc
	v_lshlrev_b32_e32 v90, 2, v22
	v_xor_b32_e32 v22, 32, v2
	v_cmp_lt_i32_e32 vcc, v22, v23
	s_mov_b32 s24, 0x10000
	v_cndmask_b32_e32 v2, v2, v22, vcc
	v_lshlrev_b32_e32 v91, 2, v2
	v_lshrrev_b32_e32 v2, 2, v79
	v_mul_u32_u24_e32 v22, 0x88, v79
	v_add3_u32 v92, v4, v22, v1
	v_or_b32_e32 v2, v88, v2
	v_lshlrev_b32_e32 v22, 3, v0
	v_mul_u32_u24_e32 v2, 0x88, v2
	v_and_b32_e32 v22, 24, v22
	v_add3_u32 v93, v4, v2, v22
	v_lshlrev_b32_e32 v2, 5, v24
	v_or3_b32 v78, v2, v1, s24
	v_bfe_u32 v2, v0, 1, 2
	v_lshrrev_b32_e32 v89, 3, v79
	v_cmp_eq_u32_e64 s[6:7], 4, v24
	v_cmp_eq_u32_e64 s[8:9], 3, v24
	v_cmp_eq_u32_e64 s[10:11], 2, v24
	v_cmp_eq_u32_e64 s[12:13], 1, v24
	v_cmp_eq_u32_e64 s[14:15], 0, v24
	v_cmp_eq_u32_e64 s[16:17], 7, v24
	v_cmp_eq_u32_e64 s[18:19], 6, v24
	v_cmp_eq_u32_e64 s[20:21], 5, v24
	v_cmp_eq_u32_e64 s[22:23], 0, v2
	v_cmp_eq_u32_e64 s[24:25], 1, v2
	v_cmp_eq_u32_e64 s[26:27], 2, v2
	v_cmp_eq_u32_e64 s[28:29], 3, v2
	s_and_b64 s[22:23], s[22:23], s[4:5]
	s_and_b64 s[24:25], s[24:25], s[4:5]
	s_and_b64 s[26:27], s[26:27], s[4:5]
	s_and_b64 s[28:29], s[28:29], s[4:5]
	v_mov_b32_e32 v71, 0xf149f2ca
	s_mov_b64 s[62:63], 0
	s_mov_b32 s69, 0xf149f2ca
	s_mov_b32 s70, 0xefa18f08
	s_mov_b32 s71, 0x41000000
	s_movk_i32 s72, 0x110
	s_mov_b32 s77, 0x26500
	s_mov_b32 s73, 0x2650c
	s_mov_b32 s80, -1
	s_mov_b32 s81, 0
	s_mov_b32 s82, 0
	s_mov_b32 s83, 0x7fffffff
	s_mov_b64 s[84:85], 0
	v_mov_b32_e32 v100, 0
	v_mov_b32_e32 v4, 0
	v_mov_b32_e32 v103, 0xf149f2ca
	v_mov_b32_e32 v46, v3
	v_mov_b32_e32 v47, v3
	v_mov_b32_e32 v48, v3
	v_mov_b32_e32 v49, v3
	v_mov_b32_e32 v50, v3
	v_mov_b32_e32 v51, v3
	v_mov_b32_e32 v52, v3
	v_mov_b32_e32 v53, v3
	v_mov_b32_e32 v38, v3
	v_mov_b32_e32 v39, v3
	v_mov_b32_e32 v40, v3
	v_mov_b32_e32 v41, v3
	v_mov_b32_e32 v42, v3
	v_mov_b32_e32 v43, v3
	v_mov_b32_e32 v44, v3
	v_mov_b32_e32 v45, v3
	v_mov_b32_e32 v30, v3
	v_mov_b32_e32 v31, v3
	v_mov_b32_e32 v32, v3
	v_mov_b32_e32 v33, v3
	v_mov_b32_e32 v34, v3
	v_mov_b32_e32 v35, v3
	v_mov_b32_e32 v36, v3
	v_mov_b32_e32 v37, v3
	v_mov_b32_e32 v22, v3
	v_mov_b32_e32 v23, v3
	v_mov_b32_e32 v24, v3
	v_mov_b32_e32 v25, v3
	v_mov_b32_e32 v26, v3
	v_mov_b32_e32 v28, v3
	v_mov_b32_e32 v29, v3
	v_readfirstlane_b32 s86, v80
	s_mov_b32 s87, 0
	v_readfirstlane_b32 s88, v99
	v_readfirstlane_b32 s89, v5
	v_readfirstlane_b32 s96, v54
	v_readfirstlane_b32 s97, v84
	v_readfirstlane_b32 s98, v85
	v_readfirstlane_b32 s99, v81
	v_readfirstlane_b32 s100, v83
	v_readfirstlane_b32 s101, v82
	s_cmp_ge_i32 s96, s68
	s_cselect_b32 s100, 0, s100
	s_branch .LBB0_95
.LBB0_95:
	s_lshl_b32 s94, s97, 4
	v_add_u32_e32 v2, s94, v79
	v_cmp_gt_i32_e32 vcc, s100, v2
	v_add_u32_e32 v2, s98, v2
	s_mov_b64 s[30:31], vcc
	v_cndmask_b32_e32 v2, 0, v2, vcc
	v_lshlrev_b32_e32 v108, 2, v2
	v_cmp_lt_i32_e32 vcc, -1, v55
	v_lshl_add_u32 v2, v55, 8, v70
	s_mov_b64 s[90:91], vcc
	v_cndmask_b32_e32 v2, v70, v2, vcc
	s_cmp_lt_i32 s86, s68
	s_cselect_b64 s[78:79], -1, 0
	s_lshl_b32 s94, s81, 4
	s_add_i32 s95, s94, 16
	s_cmp_ge_i32 s95, s83
	s_cselect_b64 s[0:1], -1, 0
	s_and_b64 s[42:43], s[78:79], s[0:1]
	s_waitcnt vmcnt(0)
	v_mov_b64_e32 v[66:67], v[74:75]
	v_mov_b64_e32 v[68:69], v[76:77]
	v_mov_b64_e32 v[62:63], v[94:95]
	v_mov_b64_e32 v[64:65], v[96:97]
	v_mov_b64_e32 v[58:59], v[120:121]
	v_mov_b64_e32 v[60:61], v[122:123]
	v_mov_b64_e32 v[54:55], v[124:125]
	v_mov_b64_e32 v[56:57], v[126:127]
	s_and_saveexec_b64 s[40:41], s[42:43]
	s_cbranch_execz .LBB0_97
	s_lshl_b32 s95, s86, 1
	v_mov_b32_e32 v99, s95
	v_or_b32_e32 v100, 1, v99
	v_min_i32_e32 v100, s67, v100
	v_cndmask_b32_e64 v99, v100, v99, s[38:39]
	v_add_u32_e32 v100, s66, v99
	v_ashrrev_i32_e32 v101, 31, v100
	v_lshlrev_b64 v[100:101], 8, v[100:101]
	v_lshl_add_u64 v[100:101], v[72:73], 0, v[100:101]
	global_load_dwordx4 v[112:115], v[100:101], off nt
.LBB0_97:
	s_or_b64 exec, exec, s[40:41]
	global_load_dword v98, v108, s[58:59]
	global_load_dwordx4 v[74:77], v2, s[92:93]
	global_load_dwordx4 v[94:97], v2, s[92:93] offset:64
	global_load_dwordx4 v[120:123], v2, s[92:93] offset:128
	global_load_dwordx4 v[124:127], v2, s[92:93] offset:192
	s_cmp_lt_i32 s80, 0
	s_cbranch_scc1 .Lattn_skip
	v_mfma_f32_16x16x32_f16 v[104:107], v[66:69], v[6:9], 0
	v_or_b32_e32 v2, s94, v79
	v_cmp_lt_i32_e64 s[42:43], v2, s82
	v_cmp_ge_i32_e64 s[40:41], v2, s82
	v_mfma_f32_16x16x32_f16 v[104:107], v[62:65], v[10:13], v[104:107]
	s_and_b64 s[42:43], s[84:85], s[42:43]
	v_cndmask_b32_e64 v2, 0, 1, s[42:43]
	s_and_b64 s[40:41], s[40:41], s[84:85]
	v_cmp_ne_u32_e64 s[42:43], 0, v2
	v_cndmask_b32_e64 v2, 0, 1, s[40:41]
	v_mfma_f32_16x16x32_f16 v[104:107], v[58:61], v[14:17], v[104:107]
	v_cmp_ne_u32_e32 vcc, 0, v2
	v_mov_b32_e32 v5, s42
	v_cmp_ngt_f32_e64 s[48:49], s70, v103
	v_mov_b32_e32 v2, vcc_lo
	v_cndmask_b32_e64 v2, v2, v5, s[38:39]
	v_mfma_f32_16x16x32_f16 v[108:111], v[54:57], v[18:21], v[104:107]
	v_lshrrev_b32_sdwa v2, v88, v2 dst_sel:DWORD dst_unused:UNUSED_PAD src0_sel:DWORD src1_sel:WORD_0
	v_and_b32_e32 v5, 1, v2
	v_cmp_eq_u32_e64 s[46:47], 0, v5
	v_and_b32_e32 v5, 2, v2
	v_cmp_eq_u32_e64 s[40:41], 0, v5
	v_and_b32_e32 v104, 4, v2
	v_and_b32_e32 v2, 8, v2
	s_nop 0
	v_cndmask_b32_e64 v107, v108, v71, s[46:47]
	v_cndmask_b32_e64 v105, v109, v71, s[40:41]
	v_cmp_eq_u32_e64 s[42:43], 0, v104
	v_cmp_eq_u32_e64 s[44:45], 0, v2
	v_max3_f32 v5, v107, s69, v105
	v_cndmask_b32_e64 v106, v110, v71, s[42:43]
	v_cndmask_b32_e64 v104, v111, v71, s[44:45]
	v_max3_f32 v2, v5, v106, v104
	ds_bpermute_b32 v5, v90, v2
	s_waitcnt lgkmcnt(0)
	v_max_f32_e32 v5, v5, v5
	v_max_f32_e32 v2, v2, v5
	ds_bpermute_b32 v5, v91, v2
	s_waitcnt lgkmcnt(0)
	v_max_f32_e32 v5, v5, v5
	v_max_f32_e32 v108, v2, v5
	v_sub_f32_e32 v2, v108, v103
	v_cmp_lt_f32_e32 vcc, s71, v2
	s_and_b64 vcc, s[48:49], vcc
	s_nop 0
	v_cndmask_b32_e64 v2, 0, 1, vcc
	v_cmp_ne_u32_e64 s[50:51], 0, v2
	s_cmp_lg_u64 s[50:51], 0
	s_cselect_b64 s[50:51], -1, 0
	s_cbranch_vccz .LBB0_117
	v_max_f32_e32 v2, v108, v108
	v_max_f32_e32 v5, v103, v103
	v_max_f32_e32 v5, v5, v2
	v_sub_f32_e32 v2, v103, v5
	v_exp_f32_e32 v2, v2
	s_cbranch_execnz .LBB0_100

.LBB0_108:
	s_or_b64 exec, exec, s[40:41]
	v_mov_b32_e32 v103, v5
	v_mov_b32_e32 v4, v54
.Lattn_skip:
	s_cmp_ge_i32 s86, s68
	s_cbranch_scc1 .LBB0_118
	s_mov_b32 s80, s86
	s_mov_b32 s81, s87
	s_mov_b32 s82, s89
	s_mov_b32 s83, s88
	s_mov_b64 s[84:85], s[90:91]
	s_mov_b32 s86, s96
	s_mov_b32 s87, s97
	s_mov_b32 s88, s100
	s_mov_b32 s89, s99
	s_waitcnt vmcnt(4)
	v_cndmask_b32_e64 v55, -1, v98, s[30:31]
	s_cmp_ge_i32 s96, s68
	s_cbranch_scc1 .LBB0_95
	s_add_i32 s97, s97, 1
	s_lshl_b32 s94, s97, 4
	s_cmp_lt_i32 s94, s100
	s_cbranch_scc1 .LBB0_95
	s_mov_b32 s97, 0
	s_mov_b32 s96, s101
	v_mov_b32_e32 v2, 0x26b40
	v_mov_b32_e32 v104, 1
	s_mov_b64 exec, 1
	ds_add_rtn_u32 v104, v2, v104
	s_mov_b64 exec, -1
	s_cmp_ge_i32 s96, s68
	s_cbranch_scc1 .Lattn_c1inv
	s_lshl_b32 s94, s96, 1
	s_min_i32 s95, s94, s67
	s_lshl_b32 s95, s95, 3
	s_add_i32 s95, s95, 0x26500
	v_mov_b32_e32 v2, s95
	ds_read_b64 v[106:107], v2
	s_or_b32 s95, s94, 1
	s_min_i32 s74, s95, s67
	s_lshl_b32 s74, s74, 3
	s_add_i32 s74, s74, 0x26504
	v_mov_b32_e32 v2, s74
	ds_read_b32 v105, v2
	s_waitcnt lgkmcnt(0)
	v_readfirstlane_b32 s101, v104
	v_readfirstlane_b32 s98, v106
	v_readfirstlane_b32 s99, v107
	v_readfirstlane_b32 s100, v105
	s_cmp_lt_i32 s95, s33
	s_cselect_b32 s100, s100, 0
	s_add_i32 s100, s100, s99
	s_branch .LBB0_95
.Lattn_c1inv:
	s_waitcnt lgkmcnt(0)
	v_readfirstlane_b32 s101, v104
	s_mov_b32 s100, 0
	s_mov_b32 s98, 0
	s_branch .LBB0_95

	.amdhsa_kernel _Z7k_attn3PKDF16_S0_PKiS2_PiPKDv8_DF16_PKfS6_S8_Pf
		.amdhsa_group_segment_fixed_size 159056
		.amdhsa_private_segment_fixed_size 0
		.amdhsa_kernarg_size 80
		.amdhsa_user_sgpr_count 2
		.amdhsa_user_sgpr_dispatch_ptr 0
		.amdhsa_user_sgpr_queue_ptr 0
		.amdhsa_user_sgpr_kernarg_segment_ptr 1
		.amdhsa_user_sgpr_dispatch_id 0
		.amdhsa_user_sgpr_kernarg_preload_length 0
		.amdhsa_user_sgpr_kernarg_preload_offset 0
		.amdhsa_user_sgpr_private_segment_size 0
		.amdhsa_uses_dynamic_stack 0
		.amdhsa_enable_private_segment 0
		.amdhsa_system_sgpr_workgroup_id_x 1
		.amdhsa_system_sgpr_workgroup_id_y 0
		.amdhsa_system_sgpr_workgroup_id_z 0
		.amdhsa_system_sgpr_workgroup_info 0
		.amdhsa_system_vgpr_workitem_id 0
		.amdhsa_next_free_vgpr 128
		.amdhsa_next_free_sgpr 102
		.amdhsa_accum_offset 128
		.amdhsa_reserve_vcc 1
		.amdhsa_float_round_mode_32 0
		.amdhsa_float_round_mode_16_64 0
		.amdhsa_float_denorm_mode_32 3
		.amdhsa_float_denorm_mode_16_64 3
		.amdhsa_dx10_clamp 1
		.amdhsa_ieee_mode 1
		.amdhsa_fp16_overflow 0
		.amdhsa_tg_split 0
		.amdhsa_exception_fp_ieee_invalid_op 0
		.amdhsa_exception_fp_denorm_src 0
		.amdhsa_exception_fp_ieee_div_zero 0
		.amdhsa_exception_fp_ieee_overflow 0
		.amdhsa_exception_fp_ieee_underflow 0
		.amdhsa_exception_fp_ieee_inexact 0
		.amdhsa_exception_int_div_zero 0
	.end_amdhsa_kernel
